# one static s_setprio 1 for waves 4-7 at kernel entry (hipcc's flips in the GQA loop kept)
# baseline (speedup 1.0000x reference)
; #define LAS __attribute__((address_space(3)))
; __global__ void __launch_bounds__(NTHR, 2) fwd_kernel(Params P) {
;     extern __shared__ __attribute__((aligned(16))) unsigned char lds[];
;     const int bid = blockIdx.x, nb = gridDim.x;
;     unsigned char* sm = lds + 16;
;     ...
;     if (threadIdx.x == 0) { ((volatile unsigned*)lds)[0] = 0u; ((volatile unsigned*)lds)[1] = 0u; ((volatile unsigned*)lds)[2] = 0u; ((volatile unsigned*)lds)[3] = 0u; }
;     __syncthreads();
;     XcdBarrier bar = xcd_barrier_post((unsigned*)P.ws, (volatile LAS unsigned*)lds);
_Z10fwd_kernel6Params:
	s_load_dwordx8 s[4:11], s[0:1], 0x140
	s_mov_b32 s44, s2
	v_readfirstlane_b32 s96, v0
	s_nop 3
	s_lshr_b32 s96, s96, 6
	s_cmp_ge_u32 s96, 4
	s_cbranch_scc0 .Lprio_done
	s_setprio 1
.Lprio_done:
	s_load_dwordx4 s[40:43], s[0:1], 0x160
	s_load_dwordx2 s[2:3], s[0:1], 0x170
	s_waitcnt lgkmcnt(0)
	v_writelane_b32 v253, s4, 0
	s_nop 1
	v_writelane_b32 v253, s5, 1
	v_writelane_b32 v253, s6, 2
	v_writelane_b32 v253, s7, 3
	v_writelane_b32 v253, s8, 4
	v_writelane_b32 v253, s9, 5
	v_writelane_b32 v253, s10, 6
	v_writelane_b32 v253, s11, 7
	v_writelane_b32 v253, s2, 8
	v_cmp_eq_u32_e64 s[4:5], 0, v0
	s_nop 0
	v_writelane_b32 v253, s3, 9
	s_load_dword s2, s[0:1], 0x178
	s_waitcnt lgkmcnt(0)
	v_writelane_b32 v253, s2, 10
	s_nop 1
	v_writelane_b32 v253, s3, 11
	s_add_u32 s2, s0, 0x178
	s_addc_u32 s3, s1, 0
	v_writelane_b32 v253, s2, 12
	s_nop 1
	v_writelane_b32 v253, s3, 13
	v_cmp_ne_u32_e64 s[2:3], 0, v0
	s_nop 1
	v_writelane_b32 v253, s2, 14
	s_nop 1
	v_writelane_b32 v253, s3, 15
	s_mov_b64 s[2:3], exec
	v_writelane_b32 v253, s4, 16
	s_nop 1
	v_writelane_b32 v253, s5, 17
	s_and_b64 s[4:5], s[2:3], s[4:5]
	s_mov_b64 exec, s[4:5]
	s_cbranch_execz .LBB0_2
	s_mov_b64 s[4:5], src_shared_base
	s_cmp_lg_u32 0, -1
	s_cselect_b32 s4, s5, 0
	s_cselect_b32 s6, 0, 0
	v_mov_b32_e32 v3, s4
	s_add_i32 s4, 0, 4
	s_cmp_lg_u32 s4, -1
	v_mov_b32_e32 v2, s6
	v_mov_b32_e32 v1, 0
	s_cselect_b32 s4, s4, 0
	flat_store_dword v[2:3], v1 sc0 sc1
	s_waitcnt vmcnt(0)
	s_cselect_b32 s6, s5, 0
	v_mov_b32_e32 v2, s4
	s_add_i32 s4, 0, 8
	s_cmp_lg_u32 s4, -1
	v_mov_b32_e32 v3, s6
	s_cselect_b32 s4, s4, 0
	flat_store_dword v[2:3], v1 sc0 sc1
	s_waitcnt vmcnt(0)
	s_cselect_b32 s6, s5, 0
	v_mov_b32_e32 v2, s4
	s_add_i32 s4, 0, 12
	s_cmp_lg_u32 s4, -1
	v_mov_b32_e32 v3, s6
	s_cselect_b32 s4, s4, 0
	s_cselect_b32 s5, s5, 0
	flat_store_dword v[2:3], v1 sc0 sc1
	s_waitcnt vmcnt(0)
	v_mov_b32_e32 v2, s4
	v_mov_b32_e32 v3, s5
	flat_store_dword v[2:3], v1 sc0 sc1
	s_waitcnt vmcnt(0)
